# nca kernels: the Wv fp32->fp16 conversions and their vmcnt waits moved out of the QK MFMA phase to just before the LDS image write (QK no longer stalls on Wv load arrival)
# speedup vs baseline: 1.0121x; 1.0097x over previous
.LBB1_16:
	s_or_b64 exec, exec, s[2:3]
	s_movk_i32 s2, 0x168
	s_waitcnt vmcnt(4)
	v_and_b32_e32 v39, 63, v0
	v_and_b32_e32 v40, 15, v0
	v_lshlrev_b32_e32 v26, 3, v50
	v_cmp_gt_u32_e32 vcc, s2, v0
	s_and_saveexec_b64 s[2:3], vcc
	s_movk_i32 s4, 0xa0
	v_mad_u32_u24 v27, v0, s4, 0
	v_mov_b32_e32 v28, 0x3c00
	ds_write_b16 v27, v28 offset:144
	s_or_b64 exec, exec, s[2:3]
	v_lshlrev_b32_e32 v38, 2, v50
	v_or_b32_e32 v28, s21, v63
	v_add_u32_e32 v29, v28, v38
	v_sub_u32_e32 v30, v38, v61
	s_movk_i32 s7, 0x80
	v_cmp_gt_u32_e64 s[2:3], 11, v30
	v_cmp_gt_u32_e64 s[4:5], s7, v29
	v_or_b32_e32 v29, 1, v38
	s_and_b64 s[2:3], s[2:3], s[4:5]
	v_mov_b32_e32 v111, 0xff800000
	v_add_u32_e32 v30, v28, v29
	v_sub_u32_e32 v29, v29, v61
	v_cndmask_b32_e64 v112, v111, 0, s[2:3]
	v_cmp_gt_u32_e64 s[2:3], 11, v29
	v_cmp_gt_u32_e64 s[4:5], s7, v30
	v_or_b32_e32 v29, 2, v38
	v_lshrrev_b32_e32 v110, 8, v0
	s_and_b64 s[2:3], s[2:3], s[4:5]
	v_add_u32_e32 v30, v28, v29
	v_sub_u32_e32 v29, v29, v61
	v_cndmask_b32_e64 v113, v111, 0, s[2:3]
	v_cmp_gt_u32_e64 s[2:3], 11, v29
	v_or_b32_e32 v29, 3, v38
	v_mad_u32_u24 v41, v110, 7, v62
	v_cmp_gt_u32_e64 s[4:5], s7, v30
	v_add_u32_e32 v28, v28, v29
	v_mad_u32_u24 v98, v41, 20, v63
	s_and_b64 s[2:3], s[2:3], s[4:5]
	v_cmp_gt_u32_e64 s[4:5], s7, v28
	v_add_u32_e32 v28, v98, v40
	s_movk_i32 s6, 0xa0
	v_mul_lo_u32 v28, v28, s6
	v_add_u32_e32 v99, 0, v28
	v_mul_u32_u24_e32 v27, 7, v110
	v_sub_u32_e32 v29, v29, v61
	v_lshl_add_u32 v94, v26, 1, v99
	s_waitcnt lgkmcnt(0)
	s_barrier
	v_cndmask_b32_e64 v114, v111, 0, s[2:3]
	v_cmp_gt_u32_e64 s[2:3], 11, v29
	ds_read_b128 v[26:29], v94
	s_and_b64 s[2:3], s[2:3], s[4:5]
	ds_read_b128 v[34:37], v94 offset:64
	v_cndmask_b32_e64 v115, v111, 0, s[2:3]
	v_cndmask_b32_e64 v30, v111, v112, s[44:45]
	v_cndmask_b32_e64 v33, v111, v115, s[44:45]
	v_cndmask_b32_e64 v32, v111, v114, s[44:45]
	v_cndmask_b32_e64 v31, v111, v113, s[44:45]
	v_cmp_gt_u32_e32 vcc, 16, v39
	v_add_u32_e32 v98, v98, v38
	s_waitcnt lgkmcnt(1)
	v_mfma_f32_16x16x32_f16 v[30:33], v[26:29], v[10:13], v[30:33]
	ds_read_b128 v[42:45], v99 offset:128
	ds_read_b128 v[46:49], v94 offset:3200
	v_cndmask_b32_e32 v29, 0, v25, vcc
	s_waitcnt lgkmcnt(2)
	v_mfma_f32_16x16x32_f16 v[30:33], v[34:37], v[2:5], v[30:33]
	v_cndmask_b32_e32 v28, 0, v24, vcc
	v_cndmask_b32_e32 v27, 0, v23, vcc
	v_cndmask_b32_e32 v26, 0, v22, vcc
	ds_read_b128 v[34:37], v94 offset:3264
	ds_read_b128 v[50:53], v99 offset:3328
	s_waitcnt lgkmcnt(3)
	v_mfma_f32_16x16x32_f16 v[22:25], v[42:45], v[26:29], v[30:33]
	ds_read_b128 v[42:45], v94 offset:6400
	ds_read_b128 v[62:65], v94 offset:6464
	v_or_b32_e32 v98, v98, v1
	v_cndmask_b32_e64 v30, v111, v112, s[46:47]
	v_cndmask_b32_e64 v33, v111, v115, s[46:47]
	v_cndmask_b32_e64 v32, v111, v114, s[46:47]
	v_cndmask_b32_e64 v31, v111, v113, s[46:47]
	v_mul_lo_u32 v98, v98, s6
	v_lshlrev_b32_e32 v61, 3, v61
	s_waitcnt lgkmcnt(4)
	v_mfma_f32_16x16x32_f16 v[30:33], v[46:49], v[10:13], v[30:33]
	ds_read_b128 v[46:49], v99 offset:6528
	ds_read_b128 v[66:69], v94 offset:9600
	v_add3_u32 v61, 0, v98, v61
	s_waitcnt lgkmcnt(5)
	v_mfma_f32_16x16x32_f16 v[30:33], v[34:37], v[2:5], v[30:33]
	v_cndmask_b32_e64 v34, v111, v112, s[48:49]
	v_cndmask_b32_e64 v37, v111, v115, s[48:49]
	v_cndmask_b32_e64 v36, v111, v114, s[48:49]
	v_cndmask_b32_e64 v35, v111, v113, s[48:49]
	ds_read_b128 v[70:73], v94 offset:9664
	ds_read_b128 v[74:77], v99 offset:9728
	s_waitcnt lgkmcnt(6)
	v_mfma_f32_16x16x32_f16 v[30:33], v[50:53], v[26:29], v[30:33]
	ds_read_b128 v[50:53], v94 offset:12800
	ds_read_b128 v[78:81], v94 offset:12864
	s_waitcnt lgkmcnt(7)
	v_mfma_f32_16x16x32_f16 v[34:37], v[42:45], v[10:13], v[34:37]
	ds_read_b128 v[42:45], v99 offset:12928
	ds_read_b128 v[82:85], v94 offset:16000
	s_waitcnt lgkmcnt(8)
	v_mfma_f32_16x16x32_f16 v[34:37], v[62:65], v[2:5], v[34:37]
	ds_read_b128 v[62:65], v94 offset:16064
	ds_read_b128 v[86:89], v99 offset:16128
	v_mul_u32_u24_e32 v128, 0xa0, v60
	s_waitcnt lgkmcnt(9)
	v_mfma_f32_16x16x32_f16 v[34:37], v[46:49], v[26:29], v[34:37]
	v_cndmask_b32_e64 v46, v111, v112, s[50:51]
	v_cndmask_b32_e64 v49, v111, v115, s[50:51]
	v_cndmask_b32_e64 v48, v111, v114, s[50:51]
	v_cndmask_b32_e64 v47, v111, v113, s[50:51]
	ds_read_b128 v[90:93], v94 offset:19200
	ds_read_b128 v[94:97], v94 offset:19264
	s_waitcnt lgkmcnt(10)
	v_mfma_f32_16x16x32_f16 v[46:49], v[66:69], v[10:13], v[46:49]
	ds_read_b128 v[66:69], v99 offset:19328
	ds_read_b64_tr_b16 v[100:101], v61 offset:3200
	v_lshlrev_b32_e32 v129, 1, v56
	s_waitcnt lgkmcnt(11)
	v_mfma_f32_16x16x32_f16 v[46:49], v[70:73], v[2:5], v[46:49]
	ds_read_b64_tr_b16 v[98:99], v61
	ds_read_b64_tr_b16 v[70:71], v61 offset:32
	s_waitcnt lgkmcnt(12)
	v_mfma_f32_16x16x32_f16 v[46:49], v[74:77], v[26:29], v[46:49]
	v_cndmask_b32_e64 v74, v111, v112, s[52:53]
	v_cndmask_b32_e64 v77, v111, v115, s[52:53]
	v_cndmask_b32_e64 v76, v111, v114, s[52:53]
	v_cndmask_b32_e64 v75, v111, v113, s[52:53]
	ds_read_b64_tr_b16 v[72:73], v61 offset:3232
	ds_read_b64_tr_b16 v[102:103], v61 offset:64
	s_waitcnt lgkmcnt(13)
	v_mfma_f32_16x16x32_f16 v[50:53], v[50:53], v[10:13], v[74:77]
	ds_read_b64_tr_b16 v[104:105], v61 offset:3264
	v_add3_u32 v128, 0, v128, v129
	s_movk_i32 s4, 0xe39
	ds_read_b64_tr_b16 v[74:75], v61 offset:96
	s_waitcnt lgkmcnt(14)
	v_mfma_f32_16x16x32_f16 v[50:53], v[78:81], v[2:5], v[50:53]
	ds_read_b64_tr_b16 v[76:77], v61 offset:3296
	ds_read_b64_tr_b16 v[78:79], v61 offset:128
	s_movk_i32 s5, 0xffee
	s_waitcnt lgkmcnt(14)
	v_mfma_f32_16x16x32_f16 v[42:45], v[42:45], v[26:29], v[50:53]
	ds_read_b64_tr_b16 v[80:81], v61 offset:3328
	ds_read_b64_tr_b16 v[106:107], v61 offset:6400
	v_cndmask_b32_e64 v50, v111, v112, s[54:55]
	v_cndmask_b32_e64 v53, v111, v115, s[54:55]
	v_cndmask_b32_e64 v52, v111, v114, s[54:55]
	v_cndmask_b32_e64 v51, v111, v113, s[54:55]
	s_nop 0
	v_mfma_f32_16x16x32_f16 v[50:53], v[82:85], v[10:13], v[50:53]
	ds_read_b64_tr_b16 v[108:109], v61 offset:9600
	ds_read_b64_tr_b16 v[82:83], v61 offset:6432
	s_waitcnt lgkmcnt(14)
	v_mfma_f32_16x16x32_f16 v[50:53], v[62:65], v[2:5], v[50:53]
	ds_read_b64_tr_b16 v[84:85], v61 offset:9632
	ds_read_b64_tr_b16 v[62:63], v61 offset:6464
	v_mfma_f32_16x16x32_f16 v[50:53], v[86:89], v[26:29], v[50:53]
	v_cndmask_b32_e64 v86, v111, v112, s[56:57]
	v_cndmask_b32_e64 v89, v111, v115, s[56:57]
	v_cndmask_b32_e64 v88, v111, v114, s[56:57]
	v_cndmask_b32_e64 v87, v111, v113, s[56:57]
	ds_read_b64_tr_b16 v[64:65], v61 offset:9664
	ds_read_b64_tr_b16 v[110:111], v61 offset:6496
	v_mfma_f32_16x16x32_f16 v[10:13], v[90:93], v[10:13], v[86:89]
	s_mov_b32 s2, 0xff800000
	ds_read_b64_tr_b16 v[112:113], v61 offset:9696
	s_nop 0
	ds_read_b64_tr_b16 v[86:87], v61 offset:6528
	v_mfma_f32_16x16x32_f16 v[2:5], v[94:97], v[2:5], v[10:13]
	ds_read_b64_tr_b16 v[88:89], v61 offset:9728
	s_nop 1
	v_max3_f32 v12, v22, s2, v23
	v_max3_f32 v12, v12, v24, v25
	v_max3_f32 v12, v12, v30, v31
	v_max3_f32 v12, v12, v32, v33
	v_max3_f32 v12, v12, v34, v35
	v_max3_f32 v12, v12, v36, v37
	v_max3_f32 v12, v12, v46, v47
	v_max3_f32 v12, v12, v48, v49
	v_mbcnt_lo_u32_b32 v13, -1, 0
	ds_read_b64_tr_b16 v[10:11], v61 offset:12800
	s_waitcnt lgkmcnt(14)
	v_mfma_f32_16x16x32_f16 v[2:5], v[66:69], v[26:29], v[2:5]
	v_max3_f32 v12, v12, v42, v43
	v_mbcnt_hi_u32_b32 v13, -1, v13
	v_max3_f32 v12, v12, v44, v45
	v_and_b32_e32 v27, 64, v13
	v_max3_f32 v12, v12, v50, v51
	v_xor_b32_e32 v26, 16, v13
	v_add_u32_e32 v27, 64, v27
	v_max3_f32 v12, v12, v52, v53
	v_cmp_lt_i32_e32 vcc, v26, v27
	v_max3_f32 v12, v12, v2, v3
	v_max3_f32 v12, v12, v4, v5
	v_mov_b32_e32 v26, v12
	s_load_dwordx2 s[2:3], s[0:1], 0x20
	s_movk_i32 s0, 0x510
	v_permlane16_swap_b32_e32 v12, v26
	v_cmp_gt_u32_e32 vcc, 11, v41
	v_mov_b32_e32 v41, 0xc80
	v_max_f32_e32 v12, v12, v26
	v_mov_b32_e32 v13, v12
	s_nop 1
	v_permlane32_swap_b32_e32 v12, v13
	s_waitcnt lgkmcnt(0)
	s_nop 0
	v_max_f32_e32 v26, v12, v13
	v_sub_f32_e32 v29, v34, v26
	v_exp_f32_e32 v92, v29
	v_sub_f32_e32 v29, v35, v26
	v_exp_f32_e32 v93, v29
	v_sub_f32_e32 v29, v36, v26
	v_exp_f32_e32 v36, v29
	v_sub_f32_e32 v29, v37, v26
	v_exp_f32_e32 v37, v29
	v_sub_f32_e32 v29, v46, v26
	v_exp_f32_e32 v94, v29
	v_sub_f32_e32 v29, v47, v26
	v_exp_f32_e32 v95, v29
	v_sub_f32_e32 v29, v48, v26
	v_sub_f32_e32 v13, v23, v26
	v_sub_f32_e32 v23, v25, v26
	v_sub_f32_e32 v25, v31, v26
	v_exp_f32_e32 v96, v29
	v_sub_f32_e32 v29, v49, v26
	v_sub_f32_e32 v12, v22, v26
	v_sub_f32_e32 v22, v24, v26
	v_sub_f32_e32 v24, v30, v26
	v_exp_f32_e32 v27, v25
	v_sub_f32_e32 v25, v32, v26
	v_sub_f32_e32 v28, v33, v26
	v_exp_f32_e32 v97, v29
	v_sub_f32_e32 v29, v42, v26
	v_exp_f32_e32 v12, v12
	v_exp_f32_e32 v13, v13
	v_exp_f32_e32 v22, v22
	v_exp_f32_e32 v23, v23
	v_exp_f32_e32 v24, v24
	v_exp_f32_e32 v25, v25
	v_exp_f32_e32 v28, v28
	v_exp_f32_e32 v114, v29
	v_sub_f32_e32 v29, v43, v26
	v_exp_f32_e32 v115, v29
	v_sub_f32_e32 v29, v44, v26
	v_exp_f32_e32 v116, v29
	v_sub_f32_e32 v29, v45, v26
	v_exp_f32_e32 v117, v29
	v_sub_f32_e32 v29, v50, v26
	v_exp_f32_e32 v118, v29
	v_sub_f32_e32 v29, v51, v26
	v_cvt_pk_f16_f32 v25, v25, v28
	v_cvt_pk_f16_f32 v24, v24, v27
	v_cvt_pk_f16_f32 v23, v22, v23
	v_cvt_pk_f16_f32 v22, v12, v13
	v_exp_f32_e32 v119, v29
	v_cndmask_b32_e32 v41, 0, v41, vcc
	v_mfma_f32_16x16x32_f16 v[28:31], v[98:101], v[22:25], 0
	ds_read_b64_tr_b16 v[12:13], v61 offset:16000
	ds_read_b64_tr_b16 v[32:33], v61 offset:12832
	v_sub_f32_e32 v27, v52, v26
	v_mfma_f32_16x16x32_f16 v[42:45], v[70:73], v[22:25], 0
	ds_read_b64_tr_b16 v[34:35], v61 offset:16032
	ds_read_b64_tr_b16 v[46:47], v61 offset:12864
	v_exp_f32_e32 v27, v27
	v_mfma_f32_16x16x32_f16 v[66:69], v[102:105], v[22:25], 0
	ds_read_b64_tr_b16 v[48:49], v61 offset:16064
	ds_read_b64_tr_b16 v[70:71], v61 offset:12896
	v_sub_f32_e32 v2, v2, v26
	v_mfma_f32_16x16x32_f16 v[74:77], v[74:77], v[22:25], 0
	ds_read_b64_tr_b16 v[72:73], v61 offset:16096
	ds_read_b64_tr_b16 v[90:91], v61 offset:12928
	v_cmp_gt_u32_e32 vcc, s0, v58
	v_mfma_f32_16x16x32_f16 v[22:25], v[78:81], v[22:25], 0
	v_cvt_pk_f16_f32 v78, v92, v93
	ds_read_b64_tr_b16 v[92:93], v61 offset:16128
	v_cvt_pk_f16_f32 v81, v96, v97
	v_cvt_pk_f16_f32 v80, v94, v95
	v_cvt_pk_f16_f32 v79, v36, v37
	v_add_u32_e32 v36, v61, v41
	v_sub_f32_e32 v37, v53, v26
	ds_read_b64_tr_b16 v[94:95], v61 offset:19200
	v_mfma_f32_16x16x32_f16 v[28:31], v[106:109], v[78:81], v[28:31]
	ds_read_b64_tr_b16 v[96:97], v36 offset:19200
	ds_read_b64_tr_b16 v[100:101], v36 offset:19232
	v_exp_f32_e32 v37, v37
	v_mfma_f32_16x16x32_f16 v[42:45], v[82:85], v[78:81], v[42:45]
	ds_read_b64_tr_b16 v[98:99], v61 offset:19232
	ds_read_b64_tr_b16 v[50:51], v61 offset:19264
	v_mfma_f32_16x16x32_f16 v[62:65], v[62:65], v[78:81], v[66:69]
	ds_read_b64_tr_b16 v[52:53], v36 offset:19264
	s_nop 1
	ds_read_b64_tr_b16 v[66:67], v61 offset:19296
	v_mfma_f32_16x16x32_f16 v[74:77], v[110:113], v[78:81], v[74:77]
	ds_read_b64_tr_b16 v[68:69], v36 offset:19296
	ds_read_b64_tr_b16 v[82:83], v61 offset:19328
	v_mfma_f32_16x16x32_f16 v[22:25], v[86:89], v[78:81], v[22:25]
	ds_read_b64_tr_b16 v[84:85], v36 offset:19328
	s_waitcnt vmcnt(2)
	v_cvt_pk_f16_f32 v21, v20, v21
	v_cvt_pk_f16_f32 v20, v18, v19
	v_cvt_pk_f16_f32 v17, v16, v17
	v_cvt_pk_f16_f32 v16, v14, v15
	ds_write_b64 v128, v[20:21] offset:57600
	v_mul_u32_u24_sdwa v18, v59, s4 dst_sel:DWORD dst_unused:UNUSED_PAD src0_sel:WORD_0 src1_sel:DWORD
	v_mul_i32_i24_sdwa v19, v18, s5 dst_sel:DWORD dst_unused:UNUSED_PAD src0_sel:WORD_1 src1_sel:DWORD
	v_mul_u32_u24_sdwa v14, v18, s6 dst_sel:DWORD dst_unused:UNUSED_PAD src0_sel:WORD_1 src1_sel:DWORD
	v_add_lshl_u32 v15, v19, v59, 3
	v_exp_f32_e32 v18, v2
	v_sub_f32_e32 v19, v3, v26
	v_sub_f32_e32 v2, v4, v26
	v_sub_f32_e32 v21, v5, v26
	v_cvt_pk_f16_f32 v81, v27, v37
	v_cvt_pk_f16_f32 v80, v118, v119
	v_cvt_pk_f16_f32 v79, v116, v117
	v_cvt_pk_f16_f32 v78, v114, v115
	v_add3_u32 v14, 0, v14, v15
	v_exp_f32_e32 v20, v2
	v_exp_f32_e32 v21, v21
	v_exp_f32_e32 v19, v19
	s_waitcnt lgkmcnt(14)
	v_mfma_f32_16x16x32_f16 v[10:13], v[10:13], v[78:81], v[28:31]
	ds_write_b64 v14, v[16:17] offset:57600
	v_mfma_f32_16x16x32_f16 v[14:17], v[32:35], v[78:81], v[42:45]
	v_mfma_f32_16x16x32_f16 v[28:31], v[46:49], v[78:81], v[62:65]
	s_nop 1
	v_mov_b32_e32 v44, 0
	v_cvt_pk_f16_f32 v43, v20, v21
	v_cvt_pk_f16_f32 v42, v18, v19
	s_waitcnt lgkmcnt(14)
	v_mfma_f32_16x16x32_f16 v[2:5], v[70:73], v[78:81], v[74:77]
	v_mov_b32_e32 v45, v44
	s_waitcnt lgkmcnt(12)
	v_mfma_f32_16x16x32_f16 v[32:35], v[90:93], v[78:81], v[22:25]
	s_waitcnt lgkmcnt(10)
	v_mfma_f32_16x16x32_f16 v[22:25], v[94:97], v[42:45], v[10:13]
	s_waitcnt lgkmcnt(8)
	v_mfma_f32_16x16x32_f16 v[18:21], v[98:101], v[42:45], v[14:17]
	s_waitcnt lgkmcnt(6)
	v_mfma_f32_16x16x32_f16 v[14:17], v[50:53], v[42:45], v[28:31]
	s_waitcnt lgkmcnt(4)
	v_mfma_f32_16x16x32_f16 v[10:13], v[66:69], v[42:45], v[2:5]
	s_waitcnt lgkmcnt(2)
	v_mfma_f32_16x16x32_f16 v[2:5], v[82:85], v[42:45], v[32:35]
	s_and_saveexec_b64 s[0:1], vcc
	s_cbranch_execz .LBB1_20
	v_mul_u32_u24_sdwa v27, v58, s4 dst_sel:DWORD dst_unused:UNUSED_PAD src0_sel:WORD_0 src1_sel:DWORD
	v_mul_i32_i24_sdwa v28, v27, s5 dst_sel:DWORD dst_unused:UNUSED_PAD src0_sel:WORD_1 src1_sel:DWORD
	s_waitcnt vmcnt(1)
	v_cvt_pk_f16_f32 v9, v8, v9
	v_cvt_pk_f16_f32 v8, v6, v7
	v_mul_u32_u24_sdwa v6, v27, s6 dst_sel:DWORD dst_unused:UNUSED_PAD src0_sel:WORD_1 src1_sel:DWORD
	v_add_lshl_u32 v7, v28, v58, 3
	v_add3_u32 v6, 0, v6, v7
	ds_write_b64 v6, v[8:9] offset:57600

.LBB2_16:
	s_or_b64 exec, exec, s[2:3]
	s_movk_i32 s2, 0x168
	s_waitcnt vmcnt(12)
	v_and_b32_e32 v38, 63, v0
	v_lshlrev_b32_e32 v26, 3, v50
	v_cmp_gt_u32_e32 vcc, s2, v0
	s_and_saveexec_b64 s[2:3], vcc
	s_movk_i32 s4, 0xa0
	v_mad_u32_u24 v27, v0, s4, 0
	v_mov_b32_e32 v28, 0x3c00
	ds_write_b16 v27, v28 offset:144
	s_or_b64 exec, exec, s[2:3]
	v_lshlrev_b32_e32 v39, 2, v50
	v_or_b32_e32 v28, s30, v57
	v_add_u32_e32 v29, v28, v39
	v_sub_u32_e32 v30, v39, v1
	s_movk_i32 s7, 0x80
	v_cmp_gt_u32_e64 s[2:3], 11, v30
	v_cmp_gt_u32_e64 s[4:5], s7, v29
	v_or_b32_e32 v29, 1, v39
	s_and_b64 s[2:3], s[2:3], s[4:5]
	v_mov_b32_e32 v51, 0xff800000
	v_add_u32_e32 v30, v28, v29
	v_sub_u32_e32 v29, v29, v1
	v_cndmask_b32_e64 v52, v51, 0, s[2:3]
	v_cmp_gt_u32_e64 s[2:3], 11, v29
	v_cmp_gt_u32_e64 s[4:5], s7, v30
	v_or_b32_e32 v29, 2, v39
	v_lshrrev_b32_e32 v41, 8, v0
	s_and_b64 s[2:3], s[2:3], s[4:5]
	v_add_u32_e32 v30, v28, v29
	v_sub_u32_e32 v29, v29, v1
	v_cndmask_b32_e64 v53, v51, 0, s[2:3]
	v_cmp_gt_u32_e64 s[2:3], 11, v29
	v_or_b32_e32 v29, 3, v39
	v_mad_u32_u24 v40, v41, 7, v76
	v_cmp_gt_u32_e64 s[4:5], s7, v30
	v_add_u32_e32 v28, v28, v29
	v_mad_u32_u24 v116, v40, 20, v57
	s_and_b64 s[2:3], s[2:3], s[4:5]
	v_cmp_gt_u32_e64 s[4:5], s7, v28
	v_add_u32_e32 v28, v116, v59
	s_movk_i32 s6, 0xa0
	v_mul_lo_u32 v28, v28, s6
	v_add_u32_e32 v117, 0, v28
	v_mul_u32_u24_e32 v27, 7, v41
	v_sub_u32_e32 v29, v29, v1
	v_lshl_add_u32 v112, v26, 1, v117
	s_waitcnt lgkmcnt(0)
	s_barrier
	v_cndmask_b32_e64 v128, v51, 0, s[2:3]
	v_cmp_gt_u32_e64 s[2:3], 11, v29
	ds_read_b128 v[26:29], v112
	s_and_b64 s[2:3], s[2:3], s[4:5]
	ds_read_b128 v[34:37], v112 offset:64
	v_cndmask_b32_e64 v129, v51, 0, s[2:3]
	v_cndmask_b32_e64 v30, v51, v52, s[44:45]
	v_cndmask_b32_e64 v33, v51, v129, s[44:45]
	v_cndmask_b32_e64 v32, v51, v128, s[44:45]
	v_cndmask_b32_e64 v31, v51, v53, s[44:45]
	v_cmp_gt_u32_e32 vcc, 16, v38
	v_add_u32_e32 v116, v116, v39
	s_waitcnt lgkmcnt(1)
	v_mfma_f32_16x16x32_f16 v[30:33], v[26:29], v[10:13], v[30:33]
	ds_read_b128 v[42:45], v117 offset:128
	ds_read_b128 v[46:49], v112 offset:3200
	v_cndmask_b32_e32 v29, 0, v25, vcc
	s_waitcnt lgkmcnt(2)
	v_mfma_f32_16x16x32_f16 v[30:33], v[34:37], v[2:5], v[30:33]
	v_cndmask_b32_e32 v28, 0, v24, vcc
	v_cndmask_b32_e32 v27, 0, v23, vcc
	v_cndmask_b32_e32 v26, 0, v22, vcc
	ds_read_b128 v[34:37], v112 offset:3264
	ds_read_b128 v[76:79], v117 offset:3328
	s_waitcnt lgkmcnt(3)
	v_mfma_f32_16x16x32_f16 v[22:25], v[42:45], v[26:29], v[30:33]
	ds_read_b128 v[42:45], v112 offset:6400
	ds_read_b128 v[80:83], v112 offset:6464
	v_or_b32_e32 v116, v116, v60
	v_cndmask_b32_e64 v30, v51, v52, s[46:47]
	v_cndmask_b32_e64 v33, v51, v129, s[46:47]
	v_cndmask_b32_e64 v32, v51, v128, s[46:47]
	v_cndmask_b32_e64 v31, v51, v53, s[46:47]
	v_mul_lo_u32 v116, v116, s6
	s_waitcnt lgkmcnt(4)
	v_mfma_f32_16x16x32_f16 v[30:33], v[46:49], v[10:13], v[30:33]
	ds_read_b128 v[46:49], v117 offset:6528
	ds_read_b128 v[84:87], v112 offset:9600
	s_waitcnt lgkmcnt(5)
	v_mfma_f32_16x16x32_f16 v[30:33], v[34:37], v[2:5], v[30:33]
	v_cndmask_b32_e64 v34, v51, v52, s[48:49]
	v_cndmask_b32_e64 v37, v51, v129, s[48:49]
	v_cndmask_b32_e64 v36, v51, v128, s[48:49]
	v_cndmask_b32_e64 v35, v51, v53, s[48:49]
	ds_read_b128 v[88:91], v112 offset:9664
	ds_read_b128 v[92:95], v117 offset:9728
	s_waitcnt lgkmcnt(6)
	v_mfma_f32_16x16x32_f16 v[30:33], v[76:79], v[26:29], v[30:33]
	ds_read_b128 v[76:79], v112 offset:12800
	ds_read_b128 v[96:99], v112 offset:12864
	v_mul_u32_u24_e32 v146, 0xa0, v75
	s_waitcnt lgkmcnt(7)
	v_mfma_f32_16x16x32_f16 v[34:37], v[42:45], v[10:13], v[34:37]
	ds_read_b128 v[42:45], v117 offset:12928
	ds_read_b128 v[100:103], v112 offset:16000
	v_lshlrev_b32_e32 v147, 1, v54
	s_waitcnt lgkmcnt(8)
	v_mfma_f32_16x16x32_f16 v[34:37], v[80:83], v[2:5], v[34:37]
	ds_read_b128 v[80:83], v112 offset:16064
	ds_read_b128 v[104:107], v117 offset:16128
	v_add3_u32 v146, 0, v146, v147
	s_waitcnt lgkmcnt(9)
	v_mfma_f32_16x16x32_f16 v[34:37], v[46:49], v[26:29], v[34:37]
	v_cndmask_b32_e64 v46, v51, v52, s[50:51]
	v_cndmask_b32_e64 v49, v51, v129, s[50:51]
	v_cndmask_b32_e64 v48, v51, v128, s[50:51]
	v_cndmask_b32_e64 v47, v51, v53, s[50:51]
	ds_read_b128 v[108:111], v112 offset:19200
	ds_read_b128 v[112:115], v112 offset:19264
	s_waitcnt lgkmcnt(10)
	v_mfma_f32_16x16x32_f16 v[46:49], v[84:87], v[10:13], v[46:49]
	ds_read_b128 v[84:87], v117 offset:19328
	v_lshlrev_b32_e32 v117, 3, v1
	v_add3_u32 v132, 0, v116, v117
	ds_read_b64_tr_b16 v[118:119], v132 offset:3200
	s_waitcnt lgkmcnt(11)
	v_mfma_f32_16x16x32_f16 v[46:49], v[88:91], v[2:5], v[46:49]
	ds_read_b64_tr_b16 v[116:117], v132
	ds_read_b64_tr_b16 v[88:89], v132 offset:32
	s_waitcnt lgkmcnt(12)
	v_mfma_f32_16x16x32_f16 v[46:49], v[92:95], v[26:29], v[46:49]
	v_cndmask_b32_e64 v92, v51, v52, s[52:53]
	v_cndmask_b32_e64 v95, v51, v129, s[52:53]
	v_cndmask_b32_e64 v94, v51, v128, s[52:53]
	v_cndmask_b32_e64 v93, v51, v53, s[52:53]
	ds_read_b64_tr_b16 v[90:91], v132 offset:3232
	ds_read_b64_tr_b16 v[120:121], v132 offset:64
	s_waitcnt lgkmcnt(13)
	v_mfma_f32_16x16x32_f16 v[76:79], v[76:79], v[10:13], v[92:95]
	ds_read_b64_tr_b16 v[122:123], v132 offset:3264
	s_movk_i32 s8, 0xffee
	ds_read_b64_tr_b16 v[92:93], v132 offset:96
	s_waitcnt lgkmcnt(14)
	v_mfma_f32_16x16x32_f16 v[76:79], v[96:99], v[2:5], v[76:79]
	ds_read_b64_tr_b16 v[94:95], v132 offset:3296
	ds_read_b64_tr_b16 v[96:97], v132 offset:128
	s_waitcnt lgkmcnt(14)
	v_mfma_f32_16x16x32_f16 v[42:45], v[42:45], v[26:29], v[76:79]
	ds_read_b64_tr_b16 v[98:99], v132 offset:3328
	ds_read_b64_tr_b16 v[124:125], v132 offset:6400
	s_movk_i32 s4, 0x510
	v_cndmask_b32_e64 v76, v51, v52, s[54:55]
	v_cndmask_b32_e64 v79, v51, v129, s[54:55]
	v_cndmask_b32_e64 v78, v51, v128, s[54:55]
	v_cndmask_b32_e64 v77, v51, v53, s[54:55]
	s_nop 0
	v_mfma_f32_16x16x32_f16 v[76:79], v[100:103], v[10:13], v[76:79]
	ds_read_b64_tr_b16 v[126:127], v132 offset:9600
	ds_read_b64_tr_b16 v[100:101], v132 offset:6432
	s_waitcnt lgkmcnt(14)
	v_mfma_f32_16x16x32_f16 v[76:79], v[80:83], v[2:5], v[76:79]
	ds_read_b64_tr_b16 v[102:103], v132 offset:9632
	ds_read_b64_tr_b16 v[80:81], v132 offset:6464
	v_mfma_f32_16x16x32_f16 v[76:79], v[104:107], v[26:29], v[76:79]
	v_cndmask_b32_e64 v104, v51, v52, s[56:57]
	v_cndmask_b32_e64 v107, v51, v129, s[56:57]
	v_cndmask_b32_e64 v106, v51, v128, s[56:57]
	v_cndmask_b32_e64 v105, v51, v53, s[56:57]
	ds_read_b64_tr_b16 v[82:83], v132 offset:9664
	ds_read_b64_tr_b16 v[128:129], v132 offset:6496
	v_mfma_f32_16x16x32_f16 v[10:13], v[108:111], v[10:13], v[104:107]
	s_mov_b32 s2, 0xff800000
	ds_read_b64_tr_b16 v[130:131], v132 offset:9696
	s_movk_i32 s7, 0xe39
	ds_read_b64_tr_b16 v[104:105], v132 offset:6528
	v_mfma_f32_16x16x32_f16 v[2:5], v[112:115], v[2:5], v[10:13]
	ds_read_b64_tr_b16 v[106:107], v132 offset:9728
	s_nop 1
	v_max3_f32 v12, v22, s2, v23
	v_max3_f32 v12, v12, v24, v25
	v_max3_f32 v12, v12, v30, v31
	v_max3_f32 v12, v12, v32, v33
	v_max3_f32 v12, v12, v34, v35
	v_max3_f32 v12, v12, v36, v37
	v_max3_f32 v12, v12, v46, v47
	v_max3_f32 v12, v12, v48, v49
	v_mbcnt_lo_u32_b32 v13, -1, 0
	ds_read_b64_tr_b16 v[10:11], v132 offset:12800
	s_waitcnt lgkmcnt(14)
	v_mfma_f32_16x16x32_f16 v[2:5], v[84:87], v[26:29], v[2:5]
	v_max3_f32 v12, v12, v42, v43
	v_mbcnt_hi_u32_b32 v13, -1, v13
	v_max3_f32 v12, v12, v44, v45
	v_and_b32_e32 v27, 64, v13
	v_max3_f32 v12, v12, v76, v77
	v_xor_b32_e32 v26, 16, v13
	v_add_u32_e32 v27, 64, v27
	v_max3_f32 v12, v12, v78, v79
	v_cmp_lt_i32_e32 vcc, v26, v27
	v_max3_f32 v12, v12, v2, v3
	v_max3_f32 v12, v12, v4, v5
	v_mov_b32_e32 v26, v12
	v_cmp_lt_u32_e64 s[2:3], 15, v38
	s_nop 0
	v_permlane16_swap_b32_e32 v12, v26
	v_cmp_gt_u32_e32 vcc, 11, v40
	s_nop 0
	v_max_f32_e32 v12, v12, v26
	v_mov_b32_e32 v13, v12
	s_nop 1
	v_permlane32_swap_b32_e32 v12, v13
	s_waitcnt lgkmcnt(0)
	s_nop 0
	v_max_f32_e32 v28, v12, v13
	v_sub_f32_e32 v12, v22, v28
	v_sub_f32_e32 v22, v24, v28
	v_sub_f32_e32 v24, v30, v28
	v_sub_f32_e32 v30, v35, v28
	v_exp_f32_e32 v41, v30
	v_sub_f32_e32 v30, v36, v28
	v_exp_f32_e32 v51, v30
	v_sub_f32_e32 v30, v37, v28
	v_exp_f32_e32 v52, v30
	v_sub_f32_e32 v30, v46, v28
	v_exp_f32_e32 v53, v30
	v_sub_f32_e32 v30, v47, v28
	v_exp_f32_e32 v110, v30
	v_sub_f32_e32 v30, v48, v28
	v_sub_f32_e32 v13, v23, v28
	v_sub_f32_e32 v23, v25, v28
	v_sub_f32_e32 v25, v31, v28
	v_exp_f32_e32 v111, v30
	v_sub_f32_e32 v30, v49, v28
	v_exp_f32_e32 v26, v25
	v_sub_f32_e32 v25, v32, v28
	v_sub_f32_e32 v27, v33, v28
	v_exp_f32_e32 v112, v30
	v_sub_f32_e32 v30, v42, v28
	v_exp_f32_e32 v12, v12
	v_exp_f32_e32 v13, v13
	v_exp_f32_e32 v22, v22
	v_exp_f32_e32 v23, v23
	v_exp_f32_e32 v24, v24
	v_exp_f32_e32 v25, v25
	v_exp_f32_e32 v27, v27
	v_exp_f32_e32 v133, v30
	v_sub_f32_e32 v30, v43, v28
	v_exp_f32_e32 v134, v30
	v_sub_f32_e32 v30, v44, v28
	v_exp_f32_e32 v135, v30
	v_sub_f32_e32 v30, v45, v28
	v_sub_f32_e32 v29, v34, v28
	v_exp_f32_e32 v136, v30
	v_sub_f32_e32 v30, v76, v28
	v_exp_f32_e32 v29, v29
	v_exp_f32_e32 v137, v30
	v_sub_f32_e32 v30, v77, v28
	v_cvt_pk_f16_f32 v25, v25, v27
	v_cvt_pk_f16_f32 v24, v24, v26
	v_cvt_pk_f16_f32 v23, v22, v23
	v_cvt_pk_f16_f32 v22, v12, v13
	v_exp_f32_e32 v138, v30
	v_mov_b32_e32 v27, 0xc80
	v_mfma_f32_16x16x32_f16 v[30:33], v[116:119], v[22:25], 0
	ds_read_b64_tr_b16 v[12:13], v132 offset:16000
	ds_read_b64_tr_b16 v[34:35], v132 offset:12832
	v_cndmask_b32_e32 v27, 0, v27, vcc
	v_mfma_f32_16x16x32_f16 v[42:45], v[88:91], v[22:25], 0
	ds_read_b64_tr_b16 v[36:37], v132 offset:16032
	ds_read_b64_tr_b16 v[46:47], v132 offset:12864
	v_sub_f32_e32 v26, v78, v28
	v_mfma_f32_16x16x32_f16 v[84:87], v[120:123], v[22:25], 0
	ds_read_b64_tr_b16 v[48:49], v132 offset:16064
	ds_read_b64_tr_b16 v[88:89], v132 offset:12896
	v_add_u32_e32 v27, v132, v27
	v_mfma_f32_16x16x32_f16 v[92:95], v[92:95], v[22:25], 0
	ds_read_b64_tr_b16 v[90:91], v132 offset:16096
	ds_read_b64_tr_b16 v[108:109], v132 offset:12928
	v_exp_f32_e32 v26, v26
	v_mfma_f32_16x16x32_f16 v[22:25], v[96:99], v[22:25], 0
	v_cvt_pk_f16_f32 v99, v111, v112
	v_cvt_pk_f16_f32 v98, v53, v110
	ds_read_b64_tr_b16 v[110:111], v132 offset:16128
	v_cvt_pk_f16_f32 v97, v51, v52
	v_cvt_pk_f16_f32 v96, v29, v41
	v_sub_f32_e32 v29, v79, v28
	ds_read_b64_tr_b16 v[112:113], v132 offset:19200
	v_mfma_f32_16x16x32_f16 v[30:33], v[124:127], v[96:99], v[30:33]
	ds_read_b64_tr_b16 v[114:115], v27 offset:19200
	ds_read_b64_tr_b16 v[118:119], v27 offset:19232
	v_exp_f32_e32 v29, v29
	v_mfma_f32_16x16x32_f16 v[40:43], v[100:103], v[96:99], v[42:45]
	ds_read_b64_tr_b16 v[116:117], v132 offset:19232
	ds_read_b64_tr_b16 v[76:77], v132 offset:19264
	v_sub_f32_e32 v2, v2, v28
	v_mfma_f32_16x16x32_f16 v[80:83], v[80:83], v[96:99], v[84:87]
	ds_read_b64_tr_b16 v[78:79], v27 offset:19264
	v_cmp_gt_u32_e32 vcc, s4, v61
	s_nop 0
	ds_read_b64_tr_b16 v[84:85], v132 offset:19296
	v_mfma_f32_16x16x32_f16 v[92:95], v[128:131], v[96:99], v[92:95]
	ds_read_b64_tr_b16 v[86:87], v27 offset:19296
	ds_read_b64_tr_b16 v[100:101], v132 offset:19328
	v_mfma_f32_16x16x32_f16 v[22:25], v[104:107], v[96:99], v[22:25]
	ds_read_b64_tr_b16 v[102:103], v27 offset:19328
	s_waitcnt vmcnt(10)
	v_cvt_pk_f16_f32 v21, v20, v21
	v_cvt_pk_f16_f32 v20, v18, v19
	v_cvt_pk_f16_f32 v17, v16, v17
	v_cvt_pk_f16_f32 v16, v14, v15
	ds_write_b64 v146, v[20:21] offset:57600
	v_mul_u32_u24_sdwa v18, v62, s7 dst_sel:DWORD dst_unused:UNUSED_PAD src0_sel:WORD_0 src1_sel:DWORD
	v_mul_i32_i24_sdwa v19, v18, s8 dst_sel:DWORD dst_unused:UNUSED_PAD src0_sel:WORD_1 src1_sel:DWORD
	v_mul_u32_u24_sdwa v14, v18, s6 dst_sel:DWORD dst_unused:UNUSED_PAD src0_sel:WORD_1 src1_sel:DWORD
	v_add_lshl_u32 v15, v19, v62, 3
	v_exp_f32_e32 v18, v2
	v_sub_f32_e32 v19, v3, v28
	v_sub_f32_e32 v2, v4, v28
	v_sub_f32_e32 v21, v5, v28
	v_cvt_pk_f16_f32 v99, v26, v29
	v_cvt_pk_f16_f32 v98, v137, v138
	v_cvt_pk_f16_f32 v97, v135, v136
	v_cvt_pk_f16_f32 v96, v133, v134
	v_add3_u32 v14, 0, v14, v15
	v_exp_f32_e32 v20, v2
	v_exp_f32_e32 v21, v21
	v_exp_f32_e32 v19, v19
	s_waitcnt lgkmcnt(14)
	v_mfma_f32_16x16x32_f16 v[10:13], v[10:13], v[96:99], v[30:33]
	ds_write_b64 v14, v[16:17] offset:57600
	v_mfma_f32_16x16x32_f16 v[14:17], v[34:37], v[96:99], v[40:43]
	v_mfma_f32_16x16x32_f16 v[30:33], v[46:49], v[96:99], v[80:83]
	s_nop 1
	v_mov_b32_e32 v42, 0
	v_cvt_pk_f16_f32 v41, v20, v21
	v_cvt_pk_f16_f32 v40, v18, v19
	s_waitcnt lgkmcnt(14)
	v_mfma_f32_16x16x32_f16 v[2:5], v[88:91], v[96:99], v[92:95]
	v_mov_b32_e32 v43, v42
	s_waitcnt lgkmcnt(12)
	v_mfma_f32_16x16x32_f16 v[34:37], v[108:111], v[96:99], v[22:25]
	s_waitcnt lgkmcnt(10)
	v_mfma_f32_16x16x32_f16 v[22:25], v[112:115], v[40:43], v[10:13]
	s_waitcnt lgkmcnt(8)
	v_mfma_f32_16x16x32_f16 v[18:21], v[116:119], v[40:43], v[14:17]
	s_waitcnt lgkmcnt(6)
	v_mfma_f32_16x16x32_f16 v[14:17], v[76:79], v[40:43], v[30:33]
	s_waitcnt lgkmcnt(4)
	v_mfma_f32_16x16x32_f16 v[10:13], v[84:87], v[40:43], v[2:5]
	s_waitcnt lgkmcnt(2)
	v_mfma_f32_16x16x32_f16 v[2:5], v[100:103], v[40:43], v[34:37]
	s_and_saveexec_b64 s[4:5], vcc
	s_cbranch_execz .LBB2_20
	v_mul_u32_u24_sdwa v26, v61, s7 dst_sel:DWORD dst_unused:UNUSED_PAD src0_sel:WORD_0 src1_sel:DWORD
	v_mul_i32_i24_sdwa v27, v26, s8 dst_sel:DWORD dst_unused:UNUSED_PAD src0_sel:WORD_1 src1_sel:DWORD
	s_waitcnt vmcnt(8)
	v_cvt_pk_f16_f32 v9, v8, v9
	v_cvt_pk_f16_f32 v8, v6, v7
	v_mul_u32_u24_sdwa v6, v26, s6 dst_sel:DWORD dst_unused:UNUSED_PAD src0_sel:WORD_1 src1_sel:DWORD
	v_add_lshl_u32 v7, v27, v61, 3
	v_add3_u32 v6, 0, v6, v7
	ds_write_b64 v6, v[8:9] offset:57600
